# nt (non-temporal) hint on the streaming row loads of P0 LN and P7 combine
# speedup vs baseline: 1.0324x; 1.0125x over previous
; #define GAS __attribute__((address_space(1)))
; __device__ __forceinline__ const GAS float* inp(const Frame& F, int i) { return (const GAS float*)*(const float* const __attribute__((address_space(4)))*)(F.ka + 8 * i); }
; __device__ __forceinline__ void ln_row(f32x4 (&v)[4], const GAS float* g, const GAS float* b, int lane) {
;     float s = 0.f;
; #pragma unroll
;     for (int j = 0; j < 4; ++j) s += (v[j].x + v[j].y) + (v[j].z + v[j].w);
;     const float mean = wave_sum(s) * (1.f / D); float s2 = 0.f;
; #pragma unroll
;     for (int j = 0; j < 4; ++j) { v[j] = v[j] - mean; s2 += (v[j].x * v[j].x + v[j].y * v[j].y) + (v[j].z * v[j].z + v[j].w * v[j].w); }
;     const float rstd = __builtin_amdgcn_rsqf(wave_sum(s2) * (1.f / D) + LN_EPS);
; __device__ __forceinline__ void p0_prologue(Frame& F) {
;     ...
;     for (int m = gw; m < M; m += NGW) { f32x4 v[4]; const GAS float* xr = inp(F, 0) + (size_t)m * D;
; #pragma unroll
;         for (int j = 0; j < 4; ++j) v[j] = *(const GAS f32x4*)(xr + 4 * F.lane + 256 * j);
;         ln_row(v, inp(F, 1), inp(F, 2), F.lane); store_row_q(v, HQ + (size_t)m * D, HS + m, F.lane); }
.LBB0_271:
	global_load_dwordx4 v[12:15], v[22:23], off offset:-2048 nt
	global_load_dwordx4 v[8:11], v[22:23], off offset:-1024 nt
	global_load_dwordx4 v[4:7], v[22:23], off nt
	global_load_dwordx4 v[0:3], v[22:23], off offset:1024 nt
	global_load_dwordx4 v[30:33], v[18:19], off
	global_load_dwordx4 v[34:37], v[18:19], off offset:1024
	global_load_dwordx4 v[38:41], v[20:21], off
	global_load_dwordx4 v[42:45], v[20:21], off offset:1024
	global_load_dwordx4 v[46:49], v[18:19], off offset:2048
	global_load_dwordx4 v[50:53], v[18:19], off offset:3072
	global_load_dwordx4 v[54:57], v[20:21], off offset:2048
	global_load_dwordx4 v[62:65], v[20:21], off offset:3072
	s_waitcnt vmcnt(11)
	v_mov_b32_e32 v66, v13
	v_mov_b32_e32 v67, v14
	v_mov_b32_e32 v68, v12
	v_mov_b32_e32 v69, v15
	s_waitcnt vmcnt(10)
	v_mov_b32_e32 v70, v9
	v_mov_b32_e32 v71, v10
	v_mov_b32_e32 v72, v8
	v_mov_b32_e32 v73, v11
	v_pk_add_f32 v[66:67], v[66:67], v[68:69]
	v_pk_add_f32 v[68:69], v[70:71], v[72:73]
	v_add_f32_e32 v29, v66, v67
	v_pk_add_f32 v[66:67], v[68:69], v[68:69] op_sel_hi:[0,1]
	s_waitcnt vmcnt(9)
	v_add_f32_e32 v75, v4, v5
	v_add_f32_e32 v77, v6, v7
	s_waitcnt vmcnt(8)
	v_mov_b32_e32 v74, v0
	v_mov_b32_e32 v76, v1
	v_mov_b32_e32 v78, v3
	v_add_f32_e32 v79, 0, v29
	v_mov_b32_e32 v66, v2
	v_pk_add_f32 v[70:71], v[74:75], v[76:77]
	v_pk_add_f32 v[66:67], v[66:67], v[78:79]
	s_nop 0
	v_pk_add_f32 v[66:67], v[70:71], v[66:67]
	s_nop 0
	v_add_f32_e32 v29, v66, v67
	v_mov_b32_e32 v58, v29
	s_nop 1
	v_mov_b32_dpp v58, v58 quad_perm:[1,0,3,2] row_mask:0xf bank_mask:0xf
	v_add_f32_e32 v29, v29, v58
	v_mov_b32_e32 v58, v29
	s_nop 1
	v_mov_b32_dpp v58, v58 quad_perm:[2,3,0,1] row_mask:0xf bank_mask:0xf
	v_add_f32_e32 v29, v29, v58
	v_mov_b32_e32 v58, v29
	s_nop 1
	v_mov_b32_dpp v58, v58 row_ror:4 row_mask:0xf bank_mask:0xf
	v_add_f32_e32 v29, v29, v58
	v_mov_b32_e32 v58, v29
	s_nop 1
	v_mov_b32_dpp v58, v58 row_ror:8 row_mask:0xf bank_mask:0xf
	v_add_f32_e32 v29, v29, v58
	v_mov_b32_e32 v58, v29
	s_nop 1
	v_mov_b32_dpp v58, v58 row_bcast:15 row_mask:0xa bank_mask:0xf
	v_add_f32_e32 v29, v29, v58
	v_mov_b32_e32 v58, v29
	s_nop 1
	v_mov_b32_dpp v58, v58 row_bcast:31 row_mask:0xc bank_mask:0xf
	v_add_f32_e32 v29, v29, v58
	s_nop 0
	v_readlane_b32 s0, v29, 63
	s_nop 1
	v_fma_f32 v13, s0, v16, v13
	v_fma_f32 v12, s0, v16, v12
	v_fma_f32 v15, s0, v16, v15
	v_fmac_f32_e32 v14, s0, v16
	v_fma_f32 v9, s0, v16, v9
	v_fma_f32 v8, s0, v16, v8
	v_fma_f32 v11, s0, v16, v11
	v_fmac_f32_e32 v10, s0, v16
	v_pk_mul_f32 v[66:67], v[14:15], v[14:15]
	v_pk_mul_f32 v[68:69], v[12:13], v[12:13]
	v_pk_mul_f32 v[70:71], v[10:11], v[10:11]
	v_pk_mul_f32 v[72:73], v[8:9], v[8:9]
	v_fma_f32 v4, s0, v16, v4
	v_fmac_f32_e32 v6, s0, v16
	v_pk_mov_b32 v[74:75], v[68:69], v[66:67] op_sel:[1,0]
	v_mov_b32_e32 v69, v67
	v_pk_mov_b32 v[66:67], v[72:73], v[70:71] op_sel:[1,0]
	v_mov_b32_e32 v73, v71
	v_fma_f32 v5, s0, v16, v5
	v_fma_f32 v7, s0, v16, v7
	v_mul_f32_e32 v58, v4, v4
	v_mul_f32_e32 v60, v6, v6
	v_pk_add_f32 v[68:69], v[74:75], v[68:69]
	v_pk_add_f32 v[66:67], v[66:67], v[72:73]
	v_fma_f32 v3, s0, v16, v3
	v_fma_f32 v2, s0, v16, v2
	v_fma_f32 v1, s0, v16, v1
	v_fmac_f32_e32 v0, s0, v16
	v_pk_fma_f32 v[70:71], v[4:5], v[4:5], v[58:59] op_sel_hi:[1,1,0]
	v_pk_fma_f32 v[76:77], v[6:7], v[6:7], v[60:61] op_sel_hi:[1,1,0]
	v_pk_add_f32 v[68:69], v[68:69], v[68:69] op_sel_hi:[0,1]
	v_pk_add_f32 v[66:67], v[66:67], v[66:67] op_sel_hi:[0,1]
	v_mul_f32_e32 v70, v0, v0
	v_mul_f32_e32 v76, v1, v1
	v_mul_f32_e32 v68, v2, v2
	v_mul_f32_e32 v66, v3, v3
	v_pk_add_f32 v[70:71], v[70:71], v[76:77]
	v_pk_add_f32 v[66:67], v[68:69], v[66:67]
	s_nop 0
	v_pk_add_f32 v[66:67], v[70:71], v[66:67]
	s_nop 0
	v_add_f32_e32 v29, v66, v67
	v_mov_b32_e32 v58, v29
	s_nop 1
	v_mov_b32_dpp v58, v58 quad_perm:[1,0,3,2] row_mask:0xf bank_mask:0xf
	v_add_f32_e32 v29, v29, v58
	v_mov_b32_e32 v58, v29
	s_nop 1
	v_mov_b32_dpp v58, v58 quad_perm:[2,3,0,1] row_mask:0xf bank_mask:0xf
	v_add_f32_e32 v29, v29, v58
	v_mov_b32_e32 v58, v29
	s_nop 1
	v_mov_b32_dpp v58, v58 row_ror:4 row_mask:0xf bank_mask:0xf
	v_add_f32_e32 v29, v29, v58
	v_mov_b32_e32 v58, v29
	s_nop 1
	v_mov_b32_dpp v58, v58 row_ror:8 row_mask:0xf bank_mask:0xf
	v_add_f32_e32 v29, v29, v58
	v_mov_b32_e32 v58, v29
	s_nop 1
	v_mov_b32_dpp v58, v58 row_bcast:15 row_mask:0xa bank_mask:0xf
	v_add_f32_e32 v29, v29, v58
	v_mov_b32_e32 v58, v29
	s_nop 1
	v_mov_b32_dpp v58, v58 row_bcast:31 row_mask:0xc bank_mask:0xf
	v_add_f32_e32 v29, v29, v58
	s_nop 0
	v_readlane_b32 s0, v29, 63
	s_nop 1
	v_fma_f32 v29, s0, v27, v26
	v_rsq_f32_e32 v58, v29
	s_nop 0
	v_pk_mul_f32 v[12:13], v[12:13], v[58:59] op_sel_hi:[1,0]
	v_pk_mul_f32 v[14:15], v[14:15], v[58:59] op_sel_hi:[1,0]
	v_pk_mul_f32 v[8:9], v[8:9], v[58:59] op_sel_hi:[1,0]
	v_pk_mul_f32 v[10:11], v[10:11], v[58:59] op_sel_hi:[1,0]
	s_waitcnt vmcnt(5)
; #define GAS __attribute__((address_space(1)))
; __device__ __forceinline__ void ln_row(f32x4 (&v)[4], const GAS float* g, const GAS float* b, int lane) {
;     ...
;     for (int j = 0; j < 4; ++j) { const f32x4 gg = *(const GAS f32x4*)(g + 4 * lane + 256 * j), bb = *(const GAS f32x4*)(b + 4 * lane + 256 * j); v[j] = v[j] * rstd * gg + bb; }
; }
; __device__ __forceinline__ float store_row_q(const f32x4 (&v)[4], GAS signed char* qrow, GAS float* hsm, int lane) {
;     float mx = 0.f;
; #pragma unroll
;     for (int j = 0; j < 4; ++j) mx = fmaxf(fmaxf(mx, fmaxf(fabsf(v[j].x), fabsf(v[j].y))), fmaxf(fabsf(v[j].z), fabsf(v[j].w)));
;     mx = wave_max(mx); const float inv = mx > 0.f ? 127.0f * __builtin_amdgcn_rcpf(mx) : 0.f;
; #pragma unroll
;     for (int j = 0; j < 4; ++j) *(GAS unsigned*)(qrow + 4 * lane + 256 * j) = pack_i8x4(v[j].x * inv, v[j].y * inv, v[j].z * inv, v[j].w * inv);
;     if (lane == 0) *hsm = mx * (1.0f / 127.0f);
;     return mx * (1.0f / 127.0f);
; }
	v_pk_fma_f32 v[14:15], v[32:33], v[14:15], v[40:41]
	v_pk_fma_f32 v[12:13], v[30:31], v[12:13], v[38:39]
	v_pk_mul_f32 v[4:5], v[4:5], v[58:59] op_sel_hi:[1,0]
	v_pk_mul_f32 v[6:7], v[6:7], v[58:59] op_sel_hi:[1,0]
	s_waitcnt vmcnt(4)
	v_pk_fma_f32 v[10:11], v[36:37], v[10:11], v[44:45]
	v_pk_fma_f32 v[8:9], v[34:35], v[8:9], v[42:43]
	v_max_f32_e64 v29, |v12|, |v13|
	v_max_f32_e64 v30, |v14|, |v15|
	v_pk_mul_f32 v[0:1], v[0:1], v[58:59] op_sel_hi:[1,0]
	v_pk_mul_f32 v[2:3], v[2:3], v[58:59] op_sel_hi:[1,0]
	s_waitcnt vmcnt(1)
	v_pk_fma_f32 v[6:7], v[48:49], v[6:7], v[56:57]
	v_pk_fma_f32 v[4:5], v[46:47], v[4:5], v[54:55]
	v_max_f32_e64 v31, |v8|, |v9|
	v_max_f32_e64 v32, |v10|, |v11|
	v_max3_f32 v29, v29, 0, v30
	s_waitcnt vmcnt(0)
	v_pk_fma_f32 v[2:3], v[2:3], v[52:53], v[64:65]
	v_pk_fma_f32 v[0:1], v[0:1], v[50:51], v[62:63]
	v_max_f32_e64 v33, |v4|, |v5|
	v_max_f32_e64 v34, |v6|, |v7|
	v_max3_f32 v29, v29, v31, v32
	v_max_f32_e64 v35, |v0|, |v1|
	v_max_f32_e64 v36, |v2|, |v3|
	v_max3_f32 v29, v29, v33, v34
	v_max3_f32 v29, v29, v35, v36
	v_mov_b32_e32 v30, v29
	s_nop 1
	v_mov_b32_dpp v30, v30 quad_perm:[1,0,3,2] row_mask:0xf bank_mask:0xf
	v_max_f32_e32 v30, v30, v30
	v_max_f32_e32 v29, v29, v30
	v_mov_b32_e32 v30, v29
	s_nop 1
	v_mov_b32_dpp v30, v30 quad_perm:[2,3,0,1] row_mask:0xf bank_mask:0xf
	v_max_f32_e32 v30, v30, v30
	v_max_f32_e32 v29, v29, v30
	v_mov_b32_e32 v30, v29
	s_nop 1
	v_mov_b32_dpp v30, v30 row_ror:4 row_mask:0xf bank_mask:0xf
	v_max_f32_e32 v30, v30, v30
	v_max_f32_e32 v29, v29, v30
	v_mov_b32_e32 v30, v29
	s_nop 1
	v_mov_b32_dpp v30, v30 row_ror:8 row_mask:0xf bank_mask:0xf
	v_max_f32_e32 v30, v30, v30
	v_max_f32_e32 v29, v29, v30
	v_mov_b32_e32 v30, v29
	s_nop 1
	v_mov_b32_dpp v30, v30 row_bcast:15 row_mask:0xa bank_mask:0xf
	v_max_f32_e32 v30, v30, v30
	v_max_f32_e32 v29, v29, v30
	v_mov_b32_e32 v30, v29
	s_nop 1
	v_mov_b32_dpp v30, v30 row_bcast:31 row_mask:0xc bank_mask:0xf
	v_max_f32_e32 v30, v30, v30
	v_max_f32_e32 v29, v29, v30
	s_nop 0
	v_readlane_b32 s3, v29, 63
	s_nop 1
	v_rcp_f32_e32 v29, s3
	v_cmp_gt_f32_e64 s[0:1], s3, 0
	v_mul_f32_e32 v29, 0x42fe0000, v29
	s_nop 0
	v_cndmask_b32_e64 v29, 0, v29, s[0:1]
	v_fmaak_f32 v13, v13, v29, 0x4b400000
	v_fmaak_f32 v14, v14, v29, 0x4b400000
	v_fmaak_f32 v9, v9, v29, 0x4b400000
	v_fmaak_f32 v10, v10, v29, 0x4b400000
	v_fmaak_f32 v5, v5, v29, 0x4b400000
	v_fmaak_f32 v6, v6, v29, 0x4b400000
	v_fmaak_f32 v1, v1, v29, 0x4b400000
	v_fmaak_f32 v2, v2, v29, 0x4b400000
	v_fmaak_f32 v12, v12, v29, 0x4b400000
	v_fmaak_f32 v15, v15, v29, 0x4b400000
	v_lshlrev_b32_e32 v13, 8, v13
	v_lshlrev_b32_e32 v14, 16, v14
	v_fmaak_f32 v8, v8, v29, 0x4b400000
	v_fmaak_f32 v11, v11, v29, 0x4b400000
	v_lshlrev_b32_e32 v9, 8, v9
	v_lshlrev_b32_e32 v10, 16, v10
	v_fmaak_f32 v4, v4, v29, 0x4b400000
	v_fmaak_f32 v7, v7, v29, 0x4b400000
	v_lshlrev_b32_e32 v5, 8, v5
	v_lshlrev_b32_e32 v6, 16, v6
	v_fmaak_f32 v0, v0, v29, 0x4b400000
	v_fmaak_f32 v3, v3, v29, 0x4b400000
	v_lshlrev_b32_e32 v1, 8, v1
	v_lshlrev_b32_e32 v2, 16, v2
	v_and_b32_e32 v13, 0xff00, v13
	v_and_b32_e32 v14, 0xff0000, v14
	v_perm_b32 v12, v15, v12, s2
	v_and_b32_e32 v9, 0xff00, v9
	v_and_b32_e32 v10, 0xff0000, v10
	v_perm_b32 v8, v11, v8, s2
	v_and_b32_e32 v5, 0xff00, v5
	v_and_b32_e32 v6, 0xff0000, v6
	v_perm_b32 v4, v7, v4, s2
	v_and_b32_e32 v1, 0xff00, v1
	v_and_b32_e32 v2, 0xff0000, v2
	v_perm_b32 v0, v3, v0, s2
	v_or3_b32 v12, v12, v13, v14
	v_or3_b32 v8, v8, v9, v10
	v_or3_b32 v4, v4, v5, v6
	v_or3_b32 v0, v0, v1, v2
	global_store_dword v[24:25], v12, off offset:-512
	global_store_dword v[24:25], v8, off offset:-256
	global_store_dword v[24:25], v4, off
	global_store_dword v[24:25], v0, off offset:256
	s_and_saveexec_b64 s[0:1], vcc
	s_cbranch_execz .LBB0_270
	v_mul_f32_e32 v0, s3, v28
	global_store_dword v17, v0, s[8:9]
	s_branch .LBB0_270

; #define GAS __attribute__((address_space(1)))
; __device__ __forceinline__ void p7_combine(Frame& F, int l) {
;     ...
;     for (int m = 4 * gw; m < M; m += 4 * NGW) {
;         f32x4 v[4][4]; unsigned hv[4][4]; float hsa[4]; unsigned yv[4][4][4];
; #pragma unroll
;         for (int r = 0; r < 4; ++r) {
; #pragma unroll
;             for (int j = 0; j < 4; ++j) hv[r][j] = *(const GAS unsigned*)(HQ + (size_t)(m + r) * D + 4 * lane + 256 * j);
;             hsa[r] = HS[m + r] * ALPHA;
; #pragma unroll
;             for (int k = 0; k < 4; ++k)
; #pragma unroll
;                 for (int j = 0; j < 4; ++j) yv[r][k][j] = *(const GAS unsigned*)(y4 + ((size_t)(m + r) * 4 + k) * D + 4 * lane + 256 * j); }
.LBB0_1055:
	v_readlane_b32 s14, v254, 50
	v_readlane_b32 s15, v254, 51
	global_load_dword v6, v[32:33], off offset:-3840 nt
	global_load_dword v8, v[32:33], off offset:-3584 nt
	global_load_dword v12, v[32:33], off offset:-3328 nt
	global_load_dword v16, v[32:33], off offset:-3072 nt
	global_load_dwordx4 v[0:3], v169, s[4:5] offset:-8
	v_lshl_add_u64 v[4:5], v[24:25], 0, s[14:15]
	global_load_dword v7, v[4:5], off nt
	global_load_dword v9, v[4:5], off offset:256 nt
	global_load_dword v13, v[4:5], off offset:512 nt
	global_load_dword v17, v[4:5], off offset:768 nt
	global_load_dword v23, v[4:5], off offset:1024 nt
	global_load_dword v10, v[4:5], off offset:1280 nt
	global_load_dword v14, v[4:5], off offset:1536 nt
	global_load_dword v18, v[4:5], off offset:1792 nt
	global_load_dword v34, v[4:5], off offset:2048 nt
	global_load_dword v11, v[4:5], off offset:2304 nt
	global_load_dword v15, v[4:5], off offset:2560 nt
	global_load_dword v19, v[4:5], off offset:2816 nt
	global_load_dword v35, v[4:5], off offset:3072 nt
	global_load_dword v22, v[4:5], off offset:3328 nt
	global_load_dword v21, v[4:5], off offset:3584 nt
	global_load_dword v20, v[4:5], off offset:3840 nt
	global_load_dword v94, v[32:33], off offset:-2816 nt
	global_load_dword v89, v[32:33], off offset:-2560 nt
	global_load_dword v84, v[32:33], off offset:-2304 nt
	global_load_dword v38, v[32:33], off offset:-2048 nt
	v_add_co_u32_e32 v36, vcc, s39, v4
	s_movk_i32 s10, 0x2000
	s_nop 0
	v_addc_co_u32_e32 v37, vcc, 0, v5, vcc
	v_add_co_u32_e32 v40, vcc, s10, v4
	s_movk_i32 s10, 0x3000
	s_nop 0
	v_addc_co_u32_e32 v41, vcc, 0, v5, vcc
	global_load_dword v95, v[40:41], off offset:-4096 nt
	global_load_dword v90, v[36:37], off offset:256 nt
	global_load_dword v85, v[36:37], off offset:512 nt
	global_load_dword v80, v[36:37], off offset:768 nt
	global_load_dword v96, v[36:37], off offset:1024 nt
	global_load_dword v91, v[36:37], off offset:1280 nt
	global_load_dword v86, v[36:37], off offset:1536 nt
	global_load_dword v81, v[36:37], off offset:1792 nt
	global_load_dword v97, v[36:37], off offset:2048 nt
	global_load_dword v92, v[36:37], off offset:2304 nt
	global_load_dword v87, v[36:37], off offset:2560 nt
	global_load_dword v82, v[36:37], off offset:2816 nt
	global_load_dword v98, v[36:37], off offset:3072 nt
	global_load_dword v93, v[36:37], off offset:3328 nt
	global_load_dword v88, v[36:37], off offset:3584 nt
	global_load_dword v83, v[36:37], off offset:3840 nt
	global_load_dword v75, v[32:33], off offset:-1792 nt
	global_load_dword v70, v[32:33], off offset:-1536 nt
	global_load_dword v65, v[32:33], off offset:-1280 nt
	global_load_dword v60, v[32:33], off offset:-1024 nt
	global_load_dword v76, v[40:41], off nt
	global_load_dword v71, v[40:41], off offset:256 nt
	global_load_dword v66, v[40:41], off offset:512 nt
	global_load_dword v61, v[40:41], off offset:768 nt
	global_load_dword v77, v[40:41], off offset:1024 nt
	global_load_dword v72, v[40:41], off offset:1280 nt
	global_load_dword v67, v[40:41], off offset:1536 nt
	global_load_dword v62, v[40:41], off offset:1792 nt
	global_load_dword v78, v[40:41], off offset:2048 nt
	global_load_dword v73, v[40:41], off offset:2304 nt
	global_load_dword v68, v[40:41], off offset:2560 nt
	global_load_dword v63, v[40:41], off offset:2816 nt
	global_load_dword v79, v[40:41], off offset:3072 nt
	global_load_dword v74, v[40:41], off offset:3328 nt
	global_load_dword v69, v[40:41], off offset:3584 nt
	global_load_dword v64, v[40:41], off offset:3840 nt
	global_load_dword v43, v[32:33], off offset:-768 nt
	global_load_dword v42, v[32:33], off offset:-512 nt
	s_nop 0
	global_load_dword v41, v[32:33], off offset:-256 nt
	global_load_dword v40, v[32:33], off nt
	v_add_co_u32_e32 v4, vcc, s10, v4
	s_mov_b32 s10, 0x3d800000
	s_nop 0
	v_addc_co_u32_e32 v5, vcc, 0, v5, vcc
	global_load_dword v56, v[4:5], off nt
	global_load_dword v52, v[4:5], off offset:256 nt
	global_load_dword v48, v[4:5], off offset:512 nt
	global_load_dword v44, v[4:5], off offset:768 nt
	global_load_dword v57, v[4:5], off offset:1024 nt
	global_load_dword v53, v[4:5], off offset:1280 nt
	global_load_dword v49, v[4:5], off offset:1536 nt
	global_load_dword v45, v[4:5], off offset:1792 nt
	global_load_dword v58, v[4:5], off offset:2048 nt
	global_load_dword v54, v[4:5], off offset:2304 nt
	global_load_dword v50, v[4:5], off offset:2560 nt
	global_load_dword v46, v[4:5], off offset:2816 nt
	global_load_dword v59, v[4:5], off offset:3072 nt
	global_load_dword v55, v[4:5], off offset:3328 nt
	global_load_dword v51, v[4:5], off offset:3584 nt
	global_load_dword v47, v[4:5], off offset:3840 nt
	v_readlane_b32 s22, v255, 10
	v_readlane_b32 s23, v255, 11
	s_andn2_b64 vcc, exec, s[22:23]
	s_waitcnt vmcnt(62)
; __device__ __forceinline__ void p7_combine(Frame& F, int l) {
;     ...
;         for (int r = 0; r < 4; ++r) {
; #pragma unroll
;             for (int j = 0; j < 4; ++j) { const int hw = (int)hv[r][j]; f32x4 a; a.x = (float)((hw << 24) >> 24) * hsa[r]; a.y = (float)((hw << 16) >> 24) * hsa[r]; a.z = (float)((hw << 8) >> 24) * hsa[r]; a.w = (float)(hw >> 24) * hsa[r];
;                 f32x4 ys = (f32x4){0.f, 0.f, 0.f, 0.f};
; #pragma unroll
;                 for (int k = 0; k < 4; ++k) { const int w = (int)yv[r][k][j]; ys.x += __builtin_amdgcn_cvt_f32_fp8(w, 0); ys.y += __builtin_amdgcn_cvt_f32_fp8(w, 1); ys.z += __builtin_amdgcn_cvt_f32_fp8(w, 2); ys.w += __builtin_amdgcn_cvt_f32_fp8(w, 3); }
;                 v[r][j] = a + ys * (1.0f / 16.0f); }
	v_cvt_f32_fp8_sdwa v36, v7 src0_sel:BYTE_2
	v_cvt_f32_fp8_sdwa v37, v7 src0_sel:BYTE_3
	v_cvt_f32_fp8_e32 v4, v7
	v_cvt_f32_fp8_sdwa v5, v7 src0_sel:BYTE_1
	v_cvt_f32_fp8_sdwa v102, v23 src0_sel:BYTE_2
	v_cvt_f32_fp8_sdwa v103, v23 src0_sel:BYTE_3
	v_cvt_f32_fp8_e32 v100, v23
	v_cvt_f32_fp8_sdwa v101, v23 src0_sel:BYTE_1
	v_cvt_f32_fp8_sdwa v106, v34 src0_sel:BYTE_2
	v_cvt_f32_fp8_sdwa v107, v34 src0_sel:BYTE_3
	v_cvt_f32_fp8_e32 v104, v34
	v_cvt_f32_fp8_sdwa v105, v34 src0_sel:BYTE_1
	v_cvt_f32_fp8_e32 v108, v35
	v_cvt_f32_fp8_sdwa v109, v35 src0_sel:BYTE_1
	v_cvt_f32_fp8_sdwa v34, v35 src0_sel:BYTE_2
	v_cvt_f32_fp8_sdwa v35, v35 src0_sel:BYTE_3
	v_pk_add_f32 v[36:37], v[36:37], 0 op_sel_hi:[1,0]
	v_pk_add_f32 v[4:5], v[4:5], 0 op_sel_hi:[1,0]
	v_pk_add_f32 v[36:37], v[36:37], v[102:103]
	v_pk_add_f32 v[4:5], v[4:5], v[100:101]
	v_pk_add_f32 v[36:37], v[36:37], v[106:107]
	v_cvt_f32_i32_sdwa v7, sext(v6) dst_sel:DWORD dst_unused:UNUSED_PAD src0_sel:BYTE_3
	v_pk_add_f32 v[34:35], v[36:37], v[34:35]
	v_cvt_f32_i32_sdwa v37, sext(v6) dst_sel:DWORD dst_unused:UNUSED_PAD src0_sel:BYTE_1
	v_cvt_f32_i32_sdwa v36, sext(v6) dst_sel:DWORD dst_unused:UNUSED_PAD src0_sel:BYTE_0
	v_cvt_f32_i32_sdwa v6, sext(v6) dst_sel:DWORD dst_unused:UNUSED_PAD src0_sel:BYTE_2
	v_pk_add_f32 v[4:5], v[4:5], v[104:105]
	v_mul_f32_e32 v0, 0x3fb504f3, v0
	v_pk_add_f32 v[4:5], v[4:5], v[108:109]
	v_cvt_f32_fp8_sdwa v102, v10 src0_sel:BYTE_2
	v_pk_mul_f32 v[100:101], v[4:5], s[10:11] op_sel_hi:[1,0]
	v_pk_mul_f32 v[4:5], v[34:35], s[10:11] op_sel_hi:[1,0]
	v_cvt_f32_fp8_e32 v34, v9
	v_pk_fma_f32 v[4:5], v[0:1], v[6:7], v[4:5] op_sel_hi:[0,1,1]
	v_pk_fma_f32 v[6:7], v[0:1], v[36:37], v[100:101] op_sel_hi:[0,1,1]
	v_cvt_f32_fp8_sdwa v35, v9 src0_sel:BYTE_1
	v_cvt_f32_fp8_sdwa v36, v9 src0_sel:BYTE_2
	v_cvt_f32_fp8_sdwa v37, v9 src0_sel:BYTE_3
	v_cvt_f32_fp8_sdwa v103, v10 src0_sel:BYTE_3
	v_cvt_f32_fp8_e32 v100, v10
	v_cvt_f32_fp8_sdwa v101, v10 src0_sel:BYTE_1
	v_cvt_f32_fp8_e32 v104, v11
	v_cvt_f32_fp8_sdwa v105, v11 src0_sel:BYTE_1
	v_cvt_f32_fp8_sdwa v10, v11 src0_sel:BYTE_2
	v_cvt_f32_fp8_sdwa v11, v11 src0_sel:BYTE_3
	v_cvt_f32_fp8_e32 v106, v22
	v_cvt_f32_fp8_sdwa v107, v22 src0_sel:BYTE_1
	v_cvt_f32_fp8_sdwa v108, v22 src0_sel:BYTE_2
	v_cvt_f32_fp8_sdwa v109, v22 src0_sel:BYTE_3
	v_pk_add_f32 v[22:23], v[34:35], 0 op_sel_hi:[1,0]
	v_pk_add_f32 v[34:35], v[36:37], 0 op_sel_hi:[1,0]
	v_pk_add_f32 v[22:23], v[22:23], v[100:101]
	v_pk_add_f32 v[34:35], v[34:35], v[102:103]
	v_cvt_f32_i32_sdwa v9, sext(v8) dst_sel:DWORD dst_unused:UNUSED_PAD src0_sel:BYTE_3
	v_pk_add_f32 v[10:11], v[34:35], v[10:11]
	v_cvt_f32_i32_sdwa v35, sext(v8) dst_sel:DWORD dst_unused:UNUSED_PAD src0_sel:BYTE_1
	v_cvt_f32_i32_sdwa v34, sext(v8) dst_sel:DWORD dst_unused:UNUSED_PAD src0_sel:BYTE_0
	v_cvt_f32_i32_sdwa v8, sext(v8) dst_sel:DWORD dst_unused:UNUSED_PAD src0_sel:BYTE_2
	v_pk_add_f32 v[22:23], v[22:23], v[104:105]
	v_pk_add_f32 v[10:11], v[10:11], v[108:109]
	v_pk_add_f32 v[22:23], v[22:23], v[106:107]
	v_pk_mul_f32 v[10:11], v[10:11], s[10:11] op_sel_hi:[1,0]
	v_pk_mul_f32 v[22:23], v[22:23], s[10:11] op_sel_hi:[1,0]
	v_pk_fma_f32 v[8:9], v[0:1], v[8:9], v[10:11] op_sel_hi:[0,1,1]
	v_pk_fma_f32 v[10:11], v[0:1], v[34:35], v[22:23] op_sel_hi:[0,1,1]
	v_cvt_f32_fp8_sdwa v34, v13 src0_sel:BYTE_2
	v_cvt_f32_fp8_sdwa v35, v13 src0_sel:BYTE_3
	v_cvt_f32_fp8_e32 v22, v13
	v_cvt_f32_fp8_sdwa v23, v13 src0_sel:BYTE_1
	v_cvt_f32_fp8_sdwa v100, v14 src0_sel:BYTE_2
	v_cvt_f32_fp8_sdwa v101, v14 src0_sel:BYTE_3
	v_cvt_f32_fp8_e32 v36, v14
	v_cvt_f32_fp8_sdwa v37, v14 src0_sel:BYTE_1
	v_cvt_f32_fp8_e32 v102, v15
	v_cvt_f32_fp8_sdwa v103, v15 src0_sel:BYTE_1
	v_cvt_f32_fp8_sdwa v14, v15 src0_sel:BYTE_2
	v_cvt_f32_fp8_sdwa v15, v15 src0_sel:BYTE_3
	s_waitcnt vmcnt(61)
	v_cvt_f32_fp8_e32 v104, v21
	v_cvt_f32_fp8_sdwa v105, v21 src0_sel:BYTE_1
	v_cvt_f32_fp8_sdwa v106, v21 src0_sel:BYTE_2
	v_cvt_f32_fp8_sdwa v107, v21 src0_sel:BYTE_3
	v_pk_add_f32 v[34:35], v[34:35], 0 op_sel_hi:[1,0]
	v_pk_add_f32 v[22:23], v[22:23], 0 op_sel_hi:[1,0]
	v_pk_add_f32 v[34:35], v[34:35], v[100:101]
	v_pk_add_f32 v[22:23], v[22:23], v[36:37]
	v_pk_add_f32 v[14:15], v[34:35], v[14:15]
	v_cvt_f32_i32_sdwa v13, sext(v12) dst_sel:DWORD dst_unused:UNUSED_PAD src0_sel:BYTE_3
	v_cvt_f32_i32_sdwa v35, sext(v12) dst_sel:DWORD dst_unused:UNUSED_PAD src0_sel:BYTE_1
	v_cvt_f32_i32_sdwa v34, sext(v12) dst_sel:DWORD dst_unused:UNUSED_PAD src0_sel:BYTE_0
	v_cvt_f32_i32_sdwa v12, sext(v12) dst_sel:DWORD dst_unused:UNUSED_PAD src0_sel:BYTE_2
	v_pk_add_f32 v[22:23], v[22:23], v[102:103]
	v_pk_add_f32 v[14:15], v[14:15], v[106:107]
	v_pk_add_f32 v[22:23], v[22:23], v[104:105]
	v_pk_mul_f32 v[14:15], v[14:15], s[10:11] op_sel_hi:[1,0]
	v_pk_mul_f32 v[22:23], v[22:23], s[10:11] op_sel_hi:[1,0]
	v_pk_fma_f32 v[12:13], v[0:1], v[12:13], v[14:15] op_sel_hi:[0,1,1]
	v_pk_fma_f32 v[14:15], v[0:1], v[34:35], v[22:23] op_sel_hi:[0,1,1]
	v_cvt_f32_fp8_e32 v22, v17
	v_cvt_f32_fp8_sdwa v23, v17 src0_sel:BYTE_1
	v_cvt_f32_fp8_sdwa v34, v17 src0_sel:BYTE_2
	v_cvt_f32_fp8_sdwa v35, v17 src0_sel:BYTE_3
	v_cvt_f32_fp8_sdwa v100, v18 src0_sel:BYTE_2
	v_cvt_f32_fp8_sdwa v101, v18 src0_sel:BYTE_3
	v_cvt_f32_fp8_e32 v36, v18
	v_cvt_f32_fp8_sdwa v37, v18 src0_sel:BYTE_1
	v_cvt_f32_fp8_e32 v102, v19
	v_cvt_f32_fp8_sdwa v103, v19 src0_sel:BYTE_1
	v_cvt_f32_fp8_sdwa v18, v19 src0_sel:BYTE_2
	v_cvt_f32_fp8_sdwa v19, v19 src0_sel:BYTE_3
	s_waitcnt vmcnt(60)
; #define GAS __attribute__((address_space(1)))
; __device__ __forceinline__ void ln_row(f32x4 (&v)[4], const GAS float* g, const GAS float* b, int lane) {
;     float s = 0.f;
; #pragma unroll
;     for (int j = 0; j < 4; ++j) s += (v[j].x + v[j].y) + (v[j].z + v[j].w);
;     const float mean = wave_sum(s) * (1.f / D); float s2 = 0.f;
; #pragma unroll
;     for (int j = 0; j < 4; ++j) { v[j] = v[j] - mean; s2 += (v[j].x * v[j].x + v[j].y * v[j].y) + (v[j].z * v[j].z + v[j].w * v[j].w); }
;     const float rstd = __builtin_amdgcn_rsqf(wave_sum(s2) * (1.f / D) + LN_EPS);
; #pragma unroll
;     for (int j = 0; j < 4; ++j) { const f32x4 gg = *(const GAS f32x4*)(g + 4 * lane + 256 * j), bb = *(const GAS f32x4*)(b + 4 * lane + 256 * j); v[j] = v[j] * rstd * gg + bb; }
; }
; __device__ __forceinline__ void p7_combine(Frame& F, int l) {
;     ...
;                 v[r][j] = a + ys * (1.0f / 16.0f); }
;             ln_row(v[r], g2, b2, lane);
;             if (lastl) store_row_f(v[r], F.H + (size_t)(m + r) * D, lane);
	v_cvt_f32_fp8_e32 v104, v20
	v_cvt_f32_fp8_sdwa v105, v20 src0_sel:BYTE_1
	v_cvt_f32_fp8_sdwa v106, v20 src0_sel:BYTE_2
	v_cvt_f32_fp8_sdwa v107, v20 src0_sel:BYTE_3
	v_pk_add_f32 v[20:21], v[22:23], 0 op_sel_hi:[1,0]
	v_pk_add_f32 v[22:23], v[34:35], 0 op_sel_hi:[1,0]
	v_cvt_f32_i32_sdwa v17, sext(v16) dst_sel:DWORD dst_unused:UNUSED_PAD src0_sel:BYTE_3
	v_pk_add_f32 v[22:23], v[22:23], v[100:101]
	v_pk_add_f32 v[20:21], v[20:21], v[36:37]
	v_pk_add_f32 v[18:19], v[22:23], v[18:19]
	v_cvt_f32_i32_sdwa v23, sext(v16) dst_sel:DWORD dst_unused:UNUSED_PAD src0_sel:BYTE_1
	v_cvt_f32_i32_sdwa v22, sext(v16) dst_sel:DWORD dst_unused:UNUSED_PAD src0_sel:BYTE_0
	v_cvt_f32_i32_sdwa v16, sext(v16) dst_sel:DWORD dst_unused:UNUSED_PAD src0_sel:BYTE_2
	v_pk_add_f32 v[20:21], v[20:21], v[102:103]
	v_pk_add_f32 v[18:19], v[18:19], v[106:107]
	v_pk_add_f32 v[20:21], v[20:21], v[104:105]
	v_pk_mul_f32 v[18:19], v[18:19], s[10:11] op_sel_hi:[1,0]
	v_pk_mul_f32 v[20:21], v[20:21], s[10:11] op_sel_hi:[1,0]
	v_pk_fma_f32 v[34:35], v[0:1], v[16:17], v[18:19] op_sel_hi:[0,1,1]
	v_pk_mov_b32 v[16:17], v[6:7], v[4:5] op_sel:[1,0]
	v_mov_b32_e32 v18, v6
	v_mov_b32_e32 v19, v5
	v_pk_fma_f32 v[36:37], v[0:1], v[22:23], v[20:21] op_sel_hi:[0,1,1]
	v_pk_add_f32 v[16:17], v[16:17], v[18:19]
	v_pk_mov_b32 v[18:19], v[10:11], v[8:9] op_sel:[1,0]
	v_mov_b32_e32 v20, v10
	v_mov_b32_e32 v21, v9
	v_pk_add_f32 v[18:19], v[18:19], v[20:21]
	v_add_f32_e32 v0, v16, v17
	v_pk_add_f32 v[18:19], v[18:19], v[18:19] op_sel:[0,1] op_sel_hi:[1,0]
	v_add_f32_e32 v16, 0, v0
	v_add_f32_e32 v20, v14, v15
	v_add_f32_e32 v22, v12, v13
	v_mov_b32_e32 v17, v36
	v_mov_b32_e32 v19, v37
	v_mov_b32_e32 v21, v34
	v_mov_b32_e32 v23, v35
	v_pk_add_f32 v[16:17], v[16:17], v[18:19]
	v_pk_add_f32 v[18:19], v[20:21], v[22:23]
	s_nop 0
	v_pk_add_f32 v[16:17], v[16:17], v[18:19]
	s_nop 0
	v_add_f32_e32 v0, v16, v17
	v_mov_b32_e32 v16, v0
	s_nop 1
	v_mov_b32_dpp v16, v16 quad_perm:[1,0,3,2] row_mask:0xf bank_mask:0xf
	v_add_f32_e32 v0, v0, v16
	v_mov_b32_e32 v16, v0
	s_nop 1
	v_mov_b32_dpp v16, v16 quad_perm:[2,3,0,1] row_mask:0xf bank_mask:0xf
	v_add_f32_e32 v0, v0, v16
	v_mov_b32_e32 v16, v0
	s_nop 1
	v_mov_b32_dpp v16, v16 row_ror:4 row_mask:0xf bank_mask:0xf
	v_add_f32_e32 v0, v0, v16
	v_mov_b32_e32 v16, v0
	s_nop 1
	v_mov_b32_dpp v16, v16 row_ror:8 row_mask:0xf bank_mask:0xf
	v_add_f32_e32 v0, v0, v16
	v_mov_b32_e32 v16, v0
	s_nop 1
	v_mov_b32_dpp v16, v16 row_bcast:15 row_mask:0xa bank_mask:0xf
	v_add_f32_e32 v0, v0, v16
	v_mov_b32_e32 v16, v0
	s_nop 1
	v_mov_b32_dpp v16, v16 row_bcast:31 row_mask:0xc bank_mask:0xf
	v_add_f32_e32 v0, v0, v16
	s_nop 0
	v_readlane_b32 s10, v0, 63
	s_nop 1
	v_fma_f32 v7, s10, v196, v7
	v_fmac_f32_e32 v6, s10, v196
	v_fma_f32 v5, s10, v196, v5
	v_fmac_f32_e32 v4, s10, v196
	v_pk_mul_f32 v[16:17], v[4:5], v[4:5]
	v_pk_mul_f32 v[18:19], v[6:7], v[6:7]
	v_fma_f32 v11, s10, v196, v11
	v_pk_mov_b32 v[20:21], v[18:19], v[16:17] op_sel:[1,0]
	v_mov_b32_e32 v19, v17
	v_fmac_f32_e32 v10, s10, v196
	v_fma_f32 v9, s10, v196, v9
	v_fmac_f32_e32 v8, s10, v196
	v_pk_add_f32 v[16:17], v[20:21], v[18:19]
	v_pk_mul_f32 v[18:19], v[8:9], v[8:9]
	v_pk_mul_f32 v[20:21], v[10:11], v[10:11]
	v_fmac_f32_e32 v14, s10, v196
	v_pk_mov_b32 v[22:23], v[20:21], v[18:19] op_sel:[1,0]
	v_mov_b32_e32 v21, v19
	v_fma_f32 v15, s10, v196, v15
	v_fmac_f32_e32 v12, s10, v196
	v_mul_f32_e32 v0, v14, v14
	v_pk_add_f32 v[18:19], v[22:23], v[20:21]
	v_fma_f32 v13, s10, v196, v13
	v_pk_fma_f32 v[20:21], v[14:15], v[14:15], v[0:1] op_sel_hi:[1,1,0]
	v_mul_f32_e32 v0, v12, v12
	v_pk_add_f32 v[16:17], v[16:17], v[16:17] op_sel_hi:[0,1]
	v_pk_add_f32 v[18:19], v[18:19], v[18:19] op_sel_hi:[0,1]
	v_pk_fma_f32 v[22:23], v[12:13], v[12:13], v[0:1] op_sel_hi:[1,1,0]
	v_fma_f32 v35, s10, v196, v35
	v_fmac_f32_e32 v34, s10, v196
	v_fma_f32 v37, s10, v196, v37
	v_fmac_f32_e32 v36, s10, v196
	v_mul_f32_e32 v20, v36, v36
	v_mul_f32_e32 v22, v37, v37
	v_mul_f32_e32 v16, v34, v34
	v_mul_f32_e32 v18, v35, v35
	v_pk_add_f32 v[20:21], v[20:21], v[22:23]
	v_pk_add_f32 v[16:17], v[16:17], v[18:19]
	s_nop 0
	v_pk_add_f32 v[16:17], v[20:21], v[16:17]
	s_nop 0
	v_add_f32_e32 v0, v16, v17
	v_mov_b32_e32 v16, v0
	s_nop 1
	v_mov_b32_dpp v16, v16 quad_perm:[1,0,3,2] row_mask:0xf bank_mask:0xf
	v_add_f32_e32 v0, v0, v16
	v_mov_b32_e32 v16, v0
	s_nop 1
	v_mov_b32_dpp v16, v16 quad_perm:[2,3,0,1] row_mask:0xf bank_mask:0xf
	v_add_f32_e32 v0, v0, v16
	v_mov_b32_e32 v16, v0
	s_nop 1
	v_mov_b32_dpp v16, v16 row_ror:4 row_mask:0xf bank_mask:0xf
	v_add_f32_e32 v0, v0, v16
	v_mov_b32_e32 v16, v0
	s_nop 1
	v_mov_b32_dpp v16, v16 row_ror:8 row_mask:0xf bank_mask:0xf
	v_add_f32_e32 v0, v0, v16
	v_mov_b32_e32 v16, v0
	s_nop 1
	v_mov_b32_dpp v16, v16 row_bcast:15 row_mask:0xa bank_mask:0xf
	v_add_f32_e32 v0, v0, v16
	v_mov_b32_e32 v16, v0
	s_nop 1
	v_mov_b32_dpp v16, v16 row_bcast:31 row_mask:0xc bank_mask:0xf
	v_add_f32_e32 v0, v0, v16
	s_nop 1
	v_readlane_b32 s10, v0, 63
	s_nop 1
	v_fma_f32 v0, s10, v197, v190
	v_rsq_f32_e32 v0, v0
	s_mov_b64 s[10:11], -1
	v_pk_mul_f32 v[100:101], v[6:7], v[0:1] op_sel_hi:[1,0]
	v_pk_mul_f32 v[4:5], v[4:5], v[0:1] op_sel_hi:[1,0]
	v_pk_mul_f32 v[8:9], v[8:9], v[0:1] op_sel_hi:[1,0]
	v_pk_mul_f32 v[12:13], v[12:13], v[0:1] op_sel_hi:[1,0]
	v_pk_mul_f32 v[36:37], v[36:37], v[0:1] op_sel_hi:[1,0]
	v_pk_mul_f32 v[34:35], v[34:35], v[0:1] op_sel_hi:[1,0]
	s_nop 0
	v_pk_fma_f32 v[6:7], v[206:207], v[4:5], v[222:223]
	v_pk_fma_f32 v[4:5], v[204:205], v[100:101], v[220:221]
	s_nop 1
	v_pk_mul_f32 v[100:101], v[10:11], v[0:1] op_sel_hi:[1,0]
	s_nop 0
	v_pk_fma_f32 v[10:11], v[210:211], v[8:9], v[226:227]
	v_pk_fma_f32 v[8:9], v[208:209], v[100:101], v[224:225]
	s_nop 1
	v_pk_mul_f32 v[100:101], v[14:15], v[0:1] op_sel_hi:[1,0]
	v_cndmask_b32_e64 v0, 0, 1, s[22:23]
	v_cmp_ne_u32_e64 s[36:37], 1, v0
	s_nop 0
	v_pk_fma_f32 v[14:15], v[214:215], v[12:13], v[230:231]
	v_pk_fma_f32 v[12:13], v[212:213], v[100:101], v[228:229]
	s_nop 1
	s_nop 0
	v_pk_fma_f32 v[18:19], v[34:35], v[218:219], v[234:235]
	v_pk_fma_f32 v[16:17], v[36:37], v[216:217], v[232:233]
	v_lshl_add_u64 v[34:35], v[30:31], 0, s[14:15]
	s_cbranch_vccnz .LBB0_1057
	s_mov_b64 s[10:11], 0
	global_store_dwordx4 v[34:35], v[4:7], off
	global_store_dwordx4 v[34:35], v[8:11], off offset:1024
	global_store_dwordx4 v[34:35], v[12:15], off offset:2048
	global_store_dwordx4 v[34:35], v[16:19], off offset:3072
